# seam-fill NW7 + seam-0 front-loading for the workgroups without an adaLN item (6 units per wave there), second measure
# speedup vs baseline: 1.0079x; 1.0079x over previous
; __device__ __forceinline__ void moe_convert(Frame& F, int lo, int hi, int rank, int nrank) {
;     if (MOE_DMA) { moe_convert_dma(F, lo, hi, rank, nrank); return; }
;     for (int it = lo + rank; it < hi; it += nrank) {
;         int r = it; const float* W; unsigned char* WT; int N, ldt, kind, off; float f8s;
;         if (r < 14336) { const int e = r / 1792; r -= e * 1792; W = F.in[IN_WMG] + (size_t)e * 2048 * DFFE; N = DFFE; WT = F.ws + WS_WGU1 + (size_t)e * 14336 * 2048; ldt = 2048; kind = 1; off = 0; f8s = 32.f; }
;         else if ((r -= 14336) < 14336) { const int e = r / 1792; r -= e * 1792; W = F.in[IN_WMU] + (size_t)e * 2048 * DFFE; N = DFFE; WT = F.ws + WS_WGU1 + (size_t)e * 14336 * 2048; ldt = 2048; kind = 1; off = 128; f8s = 256.f; }
;         else { r -= 14336; const int e = r / 1792; r -= e * 1792; W = F.in[IN_WMD] + (size_t)e * DFFE * 2048; N = 2048; WT = F.ws + WS_WDN1 + (size_t)e * 2048 * DFFE; ldt = DFFE; kind = 0; off = 0; f8s = 64.f; }
;         transpose_item_f8(W, N, WT, ldt, kind, off, r, F.lane, f8s);
;     }
.Lsf0_notw0:
	s_cmp_gt_u32 s4, 7
	s_cbranch_scc1 .Lsf0_skip
	v_mov_b32_e32 v8, 0x20020
	ds_read_b32 v9, v8 offset:4
	v_mbcnt_lo_u32_b32 v2, -1, 0
	v_mbcnt_hi_u32_b32 v2, -1, v2
	s_waitcnt lgkmcnt(0)
	v_readfirstlane_b32 s5, v9
	s_cmp_ge_u32 s5, 112
	s_cbranch_scc1 .Lsf0_skip
	s_add_i32 s5, s4, -1
	s_lshl_b32 s5, s5, 14
	v_lshl_add_u32 v7, v2, 4, s5
	ds_write_b128 v7, v[160:163] offset:0
	ds_write_b128 v7, v[164:167] offset:1024
	ds_write_b128 v7, v[168:171] offset:2048
	ds_write_b128 v7, v[172:175] offset:3072
	ds_write_b128 v7, v[176:179] offset:4096
	ds_write_b128 v7, v[180:183] offset:5120
	ds_write_b128 v7, v[184:187] offset:6144
	ds_write_b128 v7, v[188:191] offset:7168
	ds_write_b128 v7, v[192:195] offset:8192
	ds_write_b128 v7, v[196:199] offset:9216
	ds_write_b128 v7, v[200:203] offset:10240
	ds_write_b128 v7, v[204:207] offset:11264
	ds_write_b128 v7, v[208:211] offset:12288
	ds_write_b128 v7, v[212:215] offset:13312
	ds_write_b128 v7, v[216:219] offset:14336
	ds_write_b128 v7, v[220:223] offset:15360
	v_readlane_b32 s6, v247, 0
	v_readlane_b32 s7, v247, 1
	s_load_dwordx2 s[10:11], s[6:7], 0xc0
	s_load_dwordx2 s[12:13], s[6:7], 0xc8
	v_readlane_b32 s33, v247, 6
	v_mov_b32_e32 v3, 0x43e00000
	v_cmp_eq_u32_e32 vcc, 0, v2
	s_and_b32 s35, s33, 7
	s_cmp_ge_u32 s35, 6
	s_cselect_b32 s34, 6, 1
	s_mul_i32 s33, s33, 112
	s_nop 1
	v_cndmask_b32_e64 v18, 0, 1, vcc
	s_waitcnt lgkmcnt(0)
.Lsf0_loop:
	ds_add_rtn_u32 v9, v8, v18 offset:4
	s_waitcnt lgkmcnt(0)
	v_readfirstlane_b32 s18, v9
	s_cmp_ge_u32 s18, 112
	s_cbranch_scc1 .Lsf0_done
	s_add_i32 s18, s18, s33
	s_and_b32 s27, s18, 1
	s_lshr_b32 s19, s18, 1
	s_add_i32 s19, s19, 0x5000
	s_cmp_lt_u32 s19, 0x7000
	s_cbranch_scc0 .Lsf0_down
	s_add_i32 s20, s19, 0xffffc800
	s_lshr_b32 s21, s20, 8
	s_mul_i32 s21, s21, 37
	s_lshr_b32 s21, s21, 8
	s_mul_i32 s28, s21, 0x700
	s_sub_i32 s20, s20, s28
	s_mul_i32 s28, s21, 0x3800000
	s_add_u32 s14, s10, s28
	s_addc_u32 s15, s11, 0
	s_mul_i32 s28, s21, 0x1c00000
	s_add_u32 s28, s28, 0x7800000
	s_add_u32 s16, s86, s28
	s_addc_u32 s17, s87, 0
	s_movk_i32 s24, 0x7000
	s_movk_i32 s25, 0x800
	s_mov_b32 s26, 0x43800000
	s_lshr_b32 s22, s20, 4
	s_mul_i32 s22, s22, 0x2493
	s_lshr_b32 s22, s22, 16
	s_mul_i32 s28, s22, 0x70
	s_sub_i32 s23, s20, s28
	s_mov_b32 s29, 1
	s_branch .Lsf0_dec
